# router: per-batch weight build loop requests all 18 weight pieces up front (72 idle registers) and runs its 9 iterations unrolled behind counted waits instead of 9 dependent round trips
# speedup vs baseline: 1.0055x; 1.0055x over previous
.LBB0_1200:
	s_ashr_i32 s0, s31, 31
	s_lshr_b32 s0, s0, 26
	s_add_i32 s0, s31, s0
	s_ashr_i32 s26, s0, 6
	s_mul_i32 s20, s26, 0x1800
	s_ashr_i32 s21, s20, 31
	s_cmp_eq_u32 s26, s34
	s_barrier
	s_cbranch_scc1 .LBB0_1210
	s_lshl_b64 s[0:1], s[20:21], 2
	s_add_u32 s0, s28, s0
	s_addc_u32 s1, s29, s1
	s_and_saveexec_b64 s[22:23], s[38:39]
	s_cbranch_execz .LBB0_1204
	v_lshlrev_b32_e32 v114, 2, v62
	v_lshl_add_u64 v[2:3], s[0:1], 0, v[114:115]
	v_add_co_u32_e32 v4, vcc, 0x4000, v2
	s_mov_b64 s[24:25], 0x4000
	s_nop 0
	v_addc_co_u32_e32 v5, vcc, 0, v3, vcc
	global_load_dwordx4 v[10:13], v[4:5], off
	v_lshl_add_u64 v[2:3], v[2:3], 0, s[24:25]
	global_load_dwordx4 v[14:17], v[2:3], off offset:16
	s_nop 0
	global_load_dwordx4 v[2:5], v[64:65], off offset:16
	global_load_dwordx4 v[6:9], v[64:65], off
	s_mov_b64 s[24:25], 0
	v_mov_b32_e32 v18, v54
	s_waitcnt vmcnt(2)
	v_pk_add_f32 v[14:15], v[14:15], 1.0 op_sel_hi:[1,0]
	v_pk_add_f32 v[10:11], v[10:11], 1.0 op_sel_hi:[1,0]
	v_pk_add_f32 v[12:13], v[12:13], 1.0 op_sel_hi:[1,0]
	v_pk_add_f32 v[16:17], v[16:17], 1.0 op_sel_hi:[1,0]
	v_ashrrev_i32_e32 v19, 7, v18
	v_lshl_or_b32 v116, v19, 10, v62
	v_ashrrev_i32_e32 v117, 31, v116
	v_lshl_add_u64 v[116:117], v[116:117], 2, s[14:15]
	s_mov_b64 s[24:25], 0x4000
	global_load_dwordx4 v[120:123], v[116:117], off offset:16
	global_load_dwordx4 v[124:127], v[116:117], off
	v_lshl_add_u64 v[116:117], v[116:117], 0, s[24:25]
	global_load_dwordx4 v[128:131], v[116:117], off offset:16
	global_load_dwordx4 v[132:135], v[116:117], off
	v_lshl_add_u64 v[116:117], v[116:117], 0, s[24:25]
	global_load_dwordx4 v[136:139], v[116:117], off offset:16
	global_load_dwordx4 v[140:143], v[116:117], off
	v_lshl_add_u64 v[116:117], v[116:117], 0, s[24:25]
	global_load_dwordx4 v[144:147], v[116:117], off offset:16
	global_load_dwordx4 v[148:151], v[116:117], off
	v_lshl_add_u64 v[116:117], v[116:117], 0, s[24:25]
	global_load_dwordx4 v[152:155], v[116:117], off offset:16
	global_load_dwordx4 v[156:159], v[116:117], off
	v_lshl_add_u64 v[116:117], v[116:117], 0, s[24:25]
	global_load_dwordx4 v[160:163], v[116:117], off offset:16
	global_load_dwordx4 v[164:167], v[116:117], off
	v_lshl_add_u64 v[116:117], v[116:117], 0, s[24:25]
	global_load_dwordx4 v[168:171], v[116:117], off offset:16
	global_load_dwordx4 v[172:175], v[116:117], off
	v_lshl_add_u64 v[116:117], v[116:117], 0, s[24:25]
	global_load_dwordx4 v[176:179], v[116:117], off offset:16
	global_load_dwordx4 v[180:183], v[116:117], off
	v_lshl_add_u64 v[116:117], v[116:117], 0, s[24:25]
	global_load_dwordx4 v[184:187], v[116:117], off offset:16
	global_load_dwordx4 v[188:191], v[116:117], off
.LBB0_1203:
	v_ashrrev_i32_e32 v19, 7, v18
	v_bitop3_b32 v40, v19, v89, 15 bitop3:0x6c
	v_lshlrev_b32_e32 v19, 11, v19
	s_add_i32 s27, 0, 0x12000
	s_waitcnt vmcnt(16)
	v_mov_b32_e32 v20, v120
	v_mov_b32_e32 v21, v121
	v_mov_b32_e32 v22, v122
	v_mov_b32_e32 v23, v123
	v_mov_b32_e32 v24, v124
	v_mov_b32_e32 v25, v125
	v_mov_b32_e32 v26, v126
	v_mov_b32_e32 v27, v127
	v_pk_mul_f32 v[20:21], v[20:21], v[2:3]
	v_pk_mul_f32 v[24:25], v[24:25], v[6:7]
	v_pk_mul_f32 v[26:27], v[26:27], v[8:9]
	v_pk_mul_f32 v[28:29], v[24:25], v[10:11]
	s_nop 0
	v_and_b32_sdwa v30, v29, v226 dst_sel:DWORD dst_unused:UNUSED_PAD src0_sel:WORD_1 src1_sel:DWORD
	v_and_b32_sdwa v31, v28, v226 dst_sel:DWORD dst_unused:UNUSED_PAD src0_sel:WORD_1 src1_sel:DWORD
	v_add3_u32 v29, v29, v30, s9
	v_add3_u32 v28, v28, v31, s9
	v_pk_mul_f32 v[30:31], v[26:27], v[12:13]
	v_and_b32_e32 v29, 0xffff0000, v29
	v_and_b32_sdwa v32, v31, v226 dst_sel:DWORD dst_unused:UNUSED_PAD src0_sel:WORD_1 src1_sel:DWORD
	v_and_b32_sdwa v33, v30, v226 dst_sel:DWORD dst_unused:UNUSED_PAD src0_sel:WORD_1 src1_sel:DWORD
	v_add3_u32 v31, v31, v32, s9
	v_add3_u32 v30, v30, v33, s9
	v_pk_mul_f32 v[32:33], v[20:21], v[14:15]
	v_and_b32_e32 v28, 0xffff0000, v28
	v_and_b32_sdwa v34, v33, v226 dst_sel:DWORD dst_unused:UNUSED_PAD src0_sel:WORD_1 src1_sel:DWORD
	v_and_b32_sdwa v35, v32, v226 dst_sel:DWORD dst_unused:UNUSED_PAD src0_sel:WORD_1 src1_sel:DWORD
	v_add3_u32 v33, v33, v34, s9
	v_add3_u32 v32, v32, v35, s9
	v_and_b32_e32 v33, 0xffff0000, v33
	v_and_b32_e32 v32, 0xffff0000, v32
	v_pk_fma_f32 v[34:35], v[20:21], v[14:15], v[32:33] neg_lo:[0,0,1] neg_hi:[0,0,1]
	v_pk_mul_f32 v[20:21], v[22:23], v[4:5]
	v_pk_fma_f32 v[24:25], v[24:25], v[10:11], v[28:29] neg_lo:[0,0,1] neg_hi:[0,0,1]
	v_pk_mul_f32 v[22:23], v[20:21], v[16:17]
	v_and_b32_e32 v31, 0xffff0000, v31
	v_and_b32_sdwa v36, v23, v226 dst_sel:DWORD dst_unused:UNUSED_PAD src0_sel:WORD_1 src1_sel:DWORD
	v_and_b32_sdwa v37, v22, v226 dst_sel:DWORD dst_unused:UNUSED_PAD src0_sel:WORD_1 src1_sel:DWORD
	v_add3_u32 v23, v23, v36, s9
	v_add3_u32 v22, v22, v37, s9
	v_and_b32_e32 v37, 0xffff0000, v23
	v_and_b32_e32 v36, 0xffff0000, v22
	v_and_b32_e32 v30, 0xffff0000, v30
	v_pk_fma_f32 v[38:39], v[20:21], v[16:17], v[36:37] neg_lo:[0,0,1] neg_hi:[0,0,1]
	v_cvt_pk_bf16_f32 v20, v28, v29
	v_lshlrev_b32_e32 v28, 4, v40
	v_pk_fma_f32 v[26:27], v[26:27], v[12:13], v[30:31] neg_lo:[0,0,1] neg_hi:[0,0,1]
	v_cvt_pk_bf16_f32 v21, v30, v31
	v_cvt_pk_bf16_f32 v22, v32, v33
	v_cvt_pk_bf16_f32 v23, v36, v37
	v_add3_u32 v29, 0, v19, v28
	ds_write_b128 v29, v[20:23]
	v_cvt_pk_bf16_f32 v20, v24, v25
	v_cvt_pk_bf16_f32 v21, v26, v27
	v_cvt_pk_bf16_f32 v22, v34, v35
	v_cvt_pk_bf16_f32 v23, v38, v39
	v_add3_u32 v19, s27, v19, v28
	s_movk_i32 s27, 0xfff
	ds_write_b128 v19, v[20:23]
	v_add_u32_e32 v18, 0x200, v18
	v_ashrrev_i32_e32 v19, 7, v18
	v_bitop3_b32 v40, v19, v89, 15 bitop3:0x6c
	v_lshlrev_b32_e32 v19, 11, v19
	s_add_i32 s27, 0, 0x12000
	s_waitcnt vmcnt(14)
	v_mov_b32_e32 v20, v128
	v_mov_b32_e32 v21, v129
	v_mov_b32_e32 v22, v130
	v_mov_b32_e32 v23, v131
	v_mov_b32_e32 v24, v132
	v_mov_b32_e32 v25, v133
	v_mov_b32_e32 v26, v134
	v_mov_b32_e32 v27, v135
	v_pk_mul_f32 v[20:21], v[20:21], v[2:3]
	v_pk_mul_f32 v[24:25], v[24:25], v[6:7]
	v_pk_mul_f32 v[26:27], v[26:27], v[8:9]
	v_pk_mul_f32 v[28:29], v[24:25], v[10:11]
	s_nop 0
	v_and_b32_sdwa v30, v29, v226 dst_sel:DWORD dst_unused:UNUSED_PAD src0_sel:WORD_1 src1_sel:DWORD
	v_and_b32_sdwa v31, v28, v226 dst_sel:DWORD dst_unused:UNUSED_PAD src0_sel:WORD_1 src1_sel:DWORD
	v_add3_u32 v29, v29, v30, s9
	v_add3_u32 v28, v28, v31, s9
	v_pk_mul_f32 v[30:31], v[26:27], v[12:13]
	v_and_b32_e32 v29, 0xffff0000, v29
	v_and_b32_sdwa v32, v31, v226 dst_sel:DWORD dst_unused:UNUSED_PAD src0_sel:WORD_1 src1_sel:DWORD
	v_and_b32_sdwa v33, v30, v226 dst_sel:DWORD dst_unused:UNUSED_PAD src0_sel:WORD_1 src1_sel:DWORD
	v_add3_u32 v31, v31, v32, s9
	v_add3_u32 v30, v30, v33, s9
	v_pk_mul_f32 v[32:33], v[20:21], v[14:15]
	v_and_b32_e32 v28, 0xffff0000, v28
	v_and_b32_sdwa v34, v33, v226 dst_sel:DWORD dst_unused:UNUSED_PAD src0_sel:WORD_1 src1_sel:DWORD
	v_and_b32_sdwa v35, v32, v226 dst_sel:DWORD dst_unused:UNUSED_PAD src0_sel:WORD_1 src1_sel:DWORD
	v_add3_u32 v33, v33, v34, s9
	v_add3_u32 v32, v32, v35, s9
	v_and_b32_e32 v33, 0xffff0000, v33
	v_and_b32_e32 v32, 0xffff0000, v32
	v_pk_fma_f32 v[34:35], v[20:21], v[14:15], v[32:33] neg_lo:[0,0,1] neg_hi:[0,0,1]
	v_pk_mul_f32 v[20:21], v[22:23], v[4:5]
	v_pk_fma_f32 v[24:25], v[24:25], v[10:11], v[28:29] neg_lo:[0,0,1] neg_hi:[0,0,1]
	v_pk_mul_f32 v[22:23], v[20:21], v[16:17]
	v_and_b32_e32 v31, 0xffff0000, v31
	v_and_b32_sdwa v36, v23, v226 dst_sel:DWORD dst_unused:UNUSED_PAD src0_sel:WORD_1 src1_sel:DWORD
	v_and_b32_sdwa v37, v22, v226 dst_sel:DWORD dst_unused:UNUSED_PAD src0_sel:WORD_1 src1_sel:DWORD
	v_add3_u32 v23, v23, v36, s9
	v_add3_u32 v22, v22, v37, s9
	v_and_b32_e32 v37, 0xffff0000, v23
	v_and_b32_e32 v36, 0xffff0000, v22
	v_and_b32_e32 v30, 0xffff0000, v30
	v_pk_fma_f32 v[38:39], v[20:21], v[16:17], v[36:37] neg_lo:[0,0,1] neg_hi:[0,0,1]
	v_cvt_pk_bf16_f32 v20, v28, v29
	v_lshlrev_b32_e32 v28, 4, v40
	v_pk_fma_f32 v[26:27], v[26:27], v[12:13], v[30:31] neg_lo:[0,0,1] neg_hi:[0,0,1]
	v_cvt_pk_bf16_f32 v21, v30, v31
	v_cvt_pk_bf16_f32 v22, v32, v33
	v_cvt_pk_bf16_f32 v23, v36, v37
	v_add3_u32 v29, 0, v19, v28
	ds_write_b128 v29, v[20:23]
	v_cvt_pk_bf16_f32 v20, v24, v25
	v_cvt_pk_bf16_f32 v21, v26, v27
	v_cvt_pk_bf16_f32 v22, v34, v35
	v_cvt_pk_bf16_f32 v23, v38, v39
	v_add3_u32 v19, s27, v19, v28
	s_movk_i32 s27, 0xfff
	ds_write_b128 v19, v[20:23]
	v_add_u32_e32 v18, 0x200, v18
	v_ashrrev_i32_e32 v19, 7, v18
	v_bitop3_b32 v40, v19, v89, 15 bitop3:0x6c
	v_lshlrev_b32_e32 v19, 11, v19
	s_add_i32 s27, 0, 0x12000
	s_waitcnt vmcnt(12)
	v_mov_b32_e32 v20, v136
	v_mov_b32_e32 v21, v137
	v_mov_b32_e32 v22, v138
	v_mov_b32_e32 v23, v139
	v_mov_b32_e32 v24, v140
	v_mov_b32_e32 v25, v141
	v_mov_b32_e32 v26, v142
	v_mov_b32_e32 v27, v143
	v_pk_mul_f32 v[20:21], v[20:21], v[2:3]
	v_pk_mul_f32 v[24:25], v[24:25], v[6:7]
	v_pk_mul_f32 v[26:27], v[26:27], v[8:9]
	v_pk_mul_f32 v[28:29], v[24:25], v[10:11]
	s_nop 0
	v_and_b32_sdwa v30, v29, v226 dst_sel:DWORD dst_unused:UNUSED_PAD src0_sel:WORD_1 src1_sel:DWORD
	v_and_b32_sdwa v31, v28, v226 dst_sel:DWORD dst_unused:UNUSED_PAD src0_sel:WORD_1 src1_sel:DWORD
	v_add3_u32 v29, v29, v30, s9
	v_add3_u32 v28, v28, v31, s9
	v_pk_mul_f32 v[30:31], v[26:27], v[12:13]
	v_and_b32_e32 v29, 0xffff0000, v29
	v_and_b32_sdwa v32, v31, v226 dst_sel:DWORD dst_unused:UNUSED_PAD src0_sel:WORD_1 src1_sel:DWORD
	v_and_b32_sdwa v33, v30, v226 dst_sel:DWORD dst_unused:UNUSED_PAD src0_sel:WORD_1 src1_sel:DWORD
	v_add3_u32 v31, v31, v32, s9
	v_add3_u32 v30, v30, v33, s9
	v_pk_mul_f32 v[32:33], v[20:21], v[14:15]
	v_and_b32_e32 v28, 0xffff0000, v28
	v_and_b32_sdwa v34, v33, v226 dst_sel:DWORD dst_unused:UNUSED_PAD src0_sel:WORD_1 src1_sel:DWORD
	v_and_b32_sdwa v35, v32, v226 dst_sel:DWORD dst_unused:UNUSED_PAD src0_sel:WORD_1 src1_sel:DWORD
	v_add3_u32 v33, v33, v34, s9
	v_add3_u32 v32, v32, v35, s9
	v_and_b32_e32 v33, 0xffff0000, v33
	v_and_b32_e32 v32, 0xffff0000, v32
	v_pk_fma_f32 v[34:35], v[20:21], v[14:15], v[32:33] neg_lo:[0,0,1] neg_hi:[0,0,1]
	v_pk_mul_f32 v[20:21], v[22:23], v[4:5]
	v_pk_fma_f32 v[24:25], v[24:25], v[10:11], v[28:29] neg_lo:[0,0,1] neg_hi:[0,0,1]
	v_pk_mul_f32 v[22:23], v[20:21], v[16:17]
	v_and_b32_e32 v31, 0xffff0000, v31
	v_and_b32_sdwa v36, v23, v226 dst_sel:DWORD dst_unused:UNUSED_PAD src0_sel:WORD_1 src1_sel:DWORD
	v_and_b32_sdwa v37, v22, v226 dst_sel:DWORD dst_unused:UNUSED_PAD src0_sel:WORD_1 src1_sel:DWORD
	v_add3_u32 v23, v23, v36, s9
	v_add3_u32 v22, v22, v37, s9
	v_and_b32_e32 v37, 0xffff0000, v23
	v_and_b32_e32 v36, 0xffff0000, v22
	v_and_b32_e32 v30, 0xffff0000, v30
	v_pk_fma_f32 v[38:39], v[20:21], v[16:17], v[36:37] neg_lo:[0,0,1] neg_hi:[0,0,1]
	v_cvt_pk_bf16_f32 v20, v28, v29
	v_lshlrev_b32_e32 v28, 4, v40
	v_pk_fma_f32 v[26:27], v[26:27], v[12:13], v[30:31] neg_lo:[0,0,1] neg_hi:[0,0,1]
	v_cvt_pk_bf16_f32 v21, v30, v31
	v_cvt_pk_bf16_f32 v22, v32, v33
	v_cvt_pk_bf16_f32 v23, v36, v37
	v_add3_u32 v29, 0, v19, v28
	ds_write_b128 v29, v[20:23]
	v_cvt_pk_bf16_f32 v20, v24, v25
	v_cvt_pk_bf16_f32 v21, v26, v27
	v_cvt_pk_bf16_f32 v22, v34, v35
	v_cvt_pk_bf16_f32 v23, v38, v39
	v_add3_u32 v19, s27, v19, v28
	s_movk_i32 s27, 0xfff
	ds_write_b128 v19, v[20:23]
	v_add_u32_e32 v18, 0x200, v18
	v_ashrrev_i32_e32 v19, 7, v18
	v_bitop3_b32 v40, v19, v89, 15 bitop3:0x6c
	v_lshlrev_b32_e32 v19, 11, v19
	s_add_i32 s27, 0, 0x12000
	s_waitcnt vmcnt(10)
	v_mov_b32_e32 v20, v144
	v_mov_b32_e32 v21, v145
	v_mov_b32_e32 v22, v146
	v_mov_b32_e32 v23, v147
	v_mov_b32_e32 v24, v148
	v_mov_b32_e32 v25, v149
	v_mov_b32_e32 v26, v150
	v_mov_b32_e32 v27, v151
	v_pk_mul_f32 v[20:21], v[20:21], v[2:3]
	v_pk_mul_f32 v[24:25], v[24:25], v[6:7]
	v_pk_mul_f32 v[26:27], v[26:27], v[8:9]
	v_pk_mul_f32 v[28:29], v[24:25], v[10:11]
	s_nop 0
	v_and_b32_sdwa v30, v29, v226 dst_sel:DWORD dst_unused:UNUSED_PAD src0_sel:WORD_1 src1_sel:DWORD
	v_and_b32_sdwa v31, v28, v226 dst_sel:DWORD dst_unused:UNUSED_PAD src0_sel:WORD_1 src1_sel:DWORD
	v_add3_u32 v29, v29, v30, s9
	v_add3_u32 v28, v28, v31, s9
	v_pk_mul_f32 v[30:31], v[26:27], v[12:13]
	v_and_b32_e32 v29, 0xffff0000, v29
	v_and_b32_sdwa v32, v31, v226 dst_sel:DWORD dst_unused:UNUSED_PAD src0_sel:WORD_1 src1_sel:DWORD
	v_and_b32_sdwa v33, v30, v226 dst_sel:DWORD dst_unused:UNUSED_PAD src0_sel:WORD_1 src1_sel:DWORD
	v_add3_u32 v31, v31, v32, s9
	v_add3_u32 v30, v30, v33, s9
	v_pk_mul_f32 v[32:33], v[20:21], v[14:15]
	v_and_b32_e32 v28, 0xffff0000, v28
	v_and_b32_sdwa v34, v33, v226 dst_sel:DWORD dst_unused:UNUSED_PAD src0_sel:WORD_1 src1_sel:DWORD
	v_and_b32_sdwa v35, v32, v226 dst_sel:DWORD dst_unused:UNUSED_PAD src0_sel:WORD_1 src1_sel:DWORD
	v_add3_u32 v33, v33, v34, s9
	v_add3_u32 v32, v32, v35, s9
	v_and_b32_e32 v33, 0xffff0000, v33
	v_and_b32_e32 v32, 0xffff0000, v32
	v_pk_fma_f32 v[34:35], v[20:21], v[14:15], v[32:33] neg_lo:[0,0,1] neg_hi:[0,0,1]
	v_pk_mul_f32 v[20:21], v[22:23], v[4:5]
	v_pk_fma_f32 v[24:25], v[24:25], v[10:11], v[28:29] neg_lo:[0,0,1] neg_hi:[0,0,1]
	v_pk_mul_f32 v[22:23], v[20:21], v[16:17]
	v_and_b32_e32 v31, 0xffff0000, v31
	v_and_b32_sdwa v36, v23, v226 dst_sel:DWORD dst_unused:UNUSED_PAD src0_sel:WORD_1 src1_sel:DWORD
	v_and_b32_sdwa v37, v22, v226 dst_sel:DWORD dst_unused:UNUSED_PAD src0_sel:WORD_1 src1_sel:DWORD
	v_add3_u32 v23, v23, v36, s9
	v_add3_u32 v22, v22, v37, s9
	v_and_b32_e32 v37, 0xffff0000, v23
	v_and_b32_e32 v36, 0xffff0000, v22
	v_and_b32_e32 v30, 0xffff0000, v30
	v_pk_fma_f32 v[38:39], v[20:21], v[16:17], v[36:37] neg_lo:[0,0,1] neg_hi:[0,0,1]
	v_cvt_pk_bf16_f32 v20, v28, v29
	v_lshlrev_b32_e32 v28, 4, v40
	v_pk_fma_f32 v[26:27], v[26:27], v[12:13], v[30:31] neg_lo:[0,0,1] neg_hi:[0,0,1]
	v_cvt_pk_bf16_f32 v21, v30, v31
	v_cvt_pk_bf16_f32 v22, v32, v33
	v_cvt_pk_bf16_f32 v23, v36, v37
	v_add3_u32 v29, 0, v19, v28
	ds_write_b128 v29, v[20:23]
	v_cvt_pk_bf16_f32 v20, v24, v25
	v_cvt_pk_bf16_f32 v21, v26, v27
	v_cvt_pk_bf16_f32 v22, v34, v35
	v_cvt_pk_bf16_f32 v23, v38, v39
	v_add3_u32 v19, s27, v19, v28
	s_movk_i32 s27, 0xfff
	ds_write_b128 v19, v[20:23]
	v_add_u32_e32 v18, 0x200, v18
	v_ashrrev_i32_e32 v19, 7, v18
	v_bitop3_b32 v40, v19, v89, 15 bitop3:0x6c
	v_lshlrev_b32_e32 v19, 11, v19
	s_add_i32 s27, 0, 0x12000
	s_waitcnt vmcnt(8)
	v_mov_b32_e32 v20, v152
	v_mov_b32_e32 v21, v153
	v_mov_b32_e32 v22, v154
	v_mov_b32_e32 v23, v155
	v_mov_b32_e32 v24, v156
	v_mov_b32_e32 v25, v157
	v_mov_b32_e32 v26, v158
	v_mov_b32_e32 v27, v159
	v_pk_mul_f32 v[20:21], v[20:21], v[2:3]
	v_pk_mul_f32 v[24:25], v[24:25], v[6:7]
	v_pk_mul_f32 v[26:27], v[26:27], v[8:9]
	v_pk_mul_f32 v[28:29], v[24:25], v[10:11]
	s_nop 0
	v_and_b32_sdwa v30, v29, v226 dst_sel:DWORD dst_unused:UNUSED_PAD src0_sel:WORD_1 src1_sel:DWORD
	v_and_b32_sdwa v31, v28, v226 dst_sel:DWORD dst_unused:UNUSED_PAD src0_sel:WORD_1 src1_sel:DWORD
	v_add3_u32 v29, v29, v30, s9
	v_add3_u32 v28, v28, v31, s9
	v_pk_mul_f32 v[30:31], v[26:27], v[12:13]
	v_and_b32_e32 v29, 0xffff0000, v29
	v_and_b32_sdwa v32, v31, v226 dst_sel:DWORD dst_unused:UNUSED_PAD src0_sel:WORD_1 src1_sel:DWORD
	v_and_b32_sdwa v33, v30, v226 dst_sel:DWORD dst_unused:UNUSED_PAD src0_sel:WORD_1 src1_sel:DWORD
	v_add3_u32 v31, v31, v32, s9
	v_add3_u32 v30, v30, v33, s9
	v_pk_mul_f32 v[32:33], v[20:21], v[14:15]
	v_and_b32_e32 v28, 0xffff0000, v28
	v_and_b32_sdwa v34, v33, v226 dst_sel:DWORD dst_unused:UNUSED_PAD src0_sel:WORD_1 src1_sel:DWORD
	v_and_b32_sdwa v35, v32, v226 dst_sel:DWORD dst_unused:UNUSED_PAD src0_sel:WORD_1 src1_sel:DWORD
	v_add3_u32 v33, v33, v34, s9
	v_add3_u32 v32, v32, v35, s9
	v_and_b32_e32 v33, 0xffff0000, v33
	v_and_b32_e32 v32, 0xffff0000, v32
	v_pk_fma_f32 v[34:35], v[20:21], v[14:15], v[32:33] neg_lo:[0,0,1] neg_hi:[0,0,1]
	v_pk_mul_f32 v[20:21], v[22:23], v[4:5]
	v_pk_fma_f32 v[24:25], v[24:25], v[10:11], v[28:29] neg_lo:[0,0,1] neg_hi:[0,0,1]
	v_pk_mul_f32 v[22:23], v[20:21], v[16:17]
	v_and_b32_e32 v31, 0xffff0000, v31
	v_and_b32_sdwa v36, v23, v226 dst_sel:DWORD dst_unused:UNUSED_PAD src0_sel:WORD_1 src1_sel:DWORD
	v_and_b32_sdwa v37, v22, v226 dst_sel:DWORD dst_unused:UNUSED_PAD src0_sel:WORD_1 src1_sel:DWORD
	v_add3_u32 v23, v23, v36, s9
	v_add3_u32 v22, v22, v37, s9
	v_and_b32_e32 v37, 0xffff0000, v23
	v_and_b32_e32 v36, 0xffff0000, v22
	v_and_b32_e32 v30, 0xffff0000, v30
	v_pk_fma_f32 v[38:39], v[20:21], v[16:17], v[36:37] neg_lo:[0,0,1] neg_hi:[0,0,1]
	v_cvt_pk_bf16_f32 v20, v28, v29
	v_lshlrev_b32_e32 v28, 4, v40
	v_pk_fma_f32 v[26:27], v[26:27], v[12:13], v[30:31] neg_lo:[0,0,1] neg_hi:[0,0,1]
	v_cvt_pk_bf16_f32 v21, v30, v31
	v_cvt_pk_bf16_f32 v22, v32, v33
	v_cvt_pk_bf16_f32 v23, v36, v37
	v_add3_u32 v29, 0, v19, v28
	ds_write_b128 v29, v[20:23]
	v_cvt_pk_bf16_f32 v20, v24, v25
	v_cvt_pk_bf16_f32 v21, v26, v27
	v_cvt_pk_bf16_f32 v22, v34, v35
	v_cvt_pk_bf16_f32 v23, v38, v39
	v_add3_u32 v19, s27, v19, v28
	s_movk_i32 s27, 0xfff
	ds_write_b128 v19, v[20:23]
	v_add_u32_e32 v18, 0x200, v18
	v_ashrrev_i32_e32 v19, 7, v18
	v_bitop3_b32 v40, v19, v89, 15 bitop3:0x6c
	v_lshlrev_b32_e32 v19, 11, v19
	s_add_i32 s27, 0, 0x12000
	s_waitcnt vmcnt(6)
	v_mov_b32_e32 v20, v160
	v_mov_b32_e32 v21, v161
	v_mov_b32_e32 v22, v162
	v_mov_b32_e32 v23, v163
	v_mov_b32_e32 v24, v164
	v_mov_b32_e32 v25, v165
	v_mov_b32_e32 v26, v166
	v_mov_b32_e32 v27, v167
	v_pk_mul_f32 v[20:21], v[20:21], v[2:3]
	v_pk_mul_f32 v[24:25], v[24:25], v[6:7]
	v_pk_mul_f32 v[26:27], v[26:27], v[8:9]
	v_pk_mul_f32 v[28:29], v[24:25], v[10:11]
	s_nop 0
	v_and_b32_sdwa v30, v29, v226 dst_sel:DWORD dst_unused:UNUSED_PAD src0_sel:WORD_1 src1_sel:DWORD
	v_and_b32_sdwa v31, v28, v226 dst_sel:DWORD dst_unused:UNUSED_PAD src0_sel:WORD_1 src1_sel:DWORD
	v_add3_u32 v29, v29, v30, s9
	v_add3_u32 v28, v28, v31, s9
	v_pk_mul_f32 v[30:31], v[26:27], v[12:13]
	v_and_b32_e32 v29, 0xffff0000, v29
	v_and_b32_sdwa v32, v31, v226 dst_sel:DWORD dst_unused:UNUSED_PAD src0_sel:WORD_1 src1_sel:DWORD
	v_and_b32_sdwa v33, v30, v226 dst_sel:DWORD dst_unused:UNUSED_PAD src0_sel:WORD_1 src1_sel:DWORD
	v_add3_u32 v31, v31, v32, s9
	v_add3_u32 v30, v30, v33, s9
	v_pk_mul_f32 v[32:33], v[20:21], v[14:15]
	v_and_b32_e32 v28, 0xffff0000, v28
	v_and_b32_sdwa v34, v33, v226 dst_sel:DWORD dst_unused:UNUSED_PAD src0_sel:WORD_1 src1_sel:DWORD
	v_and_b32_sdwa v35, v32, v226 dst_sel:DWORD dst_unused:UNUSED_PAD src0_sel:WORD_1 src1_sel:DWORD
	v_add3_u32 v33, v33, v34, s9
	v_add3_u32 v32, v32, v35, s9
	v_and_b32_e32 v33, 0xffff0000, v33
	v_and_b32_e32 v32, 0xffff0000, v32
	v_pk_fma_f32 v[34:35], v[20:21], v[14:15], v[32:33] neg_lo:[0,0,1] neg_hi:[0,0,1]
	v_pk_mul_f32 v[20:21], v[22:23], v[4:5]
	v_pk_fma_f32 v[24:25], v[24:25], v[10:11], v[28:29] neg_lo:[0,0,1] neg_hi:[0,0,1]
	v_pk_mul_f32 v[22:23], v[20:21], v[16:17]
	v_and_b32_e32 v31, 0xffff0000, v31
	v_and_b32_sdwa v36, v23, v226 dst_sel:DWORD dst_unused:UNUSED_PAD src0_sel:WORD_1 src1_sel:DWORD
	v_and_b32_sdwa v37, v22, v226 dst_sel:DWORD dst_unused:UNUSED_PAD src0_sel:WORD_1 src1_sel:DWORD
	v_add3_u32 v23, v23, v36, s9
	v_add3_u32 v22, v22, v37, s9
	v_and_b32_e32 v37, 0xffff0000, v23
	v_and_b32_e32 v36, 0xffff0000, v22
	v_and_b32_e32 v30, 0xffff0000, v30
	v_pk_fma_f32 v[38:39], v[20:21], v[16:17], v[36:37] neg_lo:[0,0,1] neg_hi:[0,0,1]
	v_cvt_pk_bf16_f32 v20, v28, v29
	v_lshlrev_b32_e32 v28, 4, v40
	v_pk_fma_f32 v[26:27], v[26:27], v[12:13], v[30:31] neg_lo:[0,0,1] neg_hi:[0,0,1]
	v_cvt_pk_bf16_f32 v21, v30, v31
	v_cvt_pk_bf16_f32 v22, v32, v33
	v_cvt_pk_bf16_f32 v23, v36, v37
	v_add3_u32 v29, 0, v19, v28
	ds_write_b128 v29, v[20:23]
	v_cvt_pk_bf16_f32 v20, v24, v25
	v_cvt_pk_bf16_f32 v21, v26, v27
	v_cvt_pk_bf16_f32 v22, v34, v35
	v_cvt_pk_bf16_f32 v23, v38, v39
	v_add3_u32 v19, s27, v19, v28
	s_movk_i32 s27, 0xfff
	ds_write_b128 v19, v[20:23]
	v_add_u32_e32 v18, 0x200, v18
	v_ashrrev_i32_e32 v19, 7, v18
	v_bitop3_b32 v40, v19, v89, 15 bitop3:0x6c
	v_lshlrev_b32_e32 v19, 11, v19
	s_add_i32 s27, 0, 0x12000
	s_waitcnt vmcnt(4)
	v_mov_b32_e32 v20, v168
	v_mov_b32_e32 v21, v169
	v_mov_b32_e32 v22, v170
	v_mov_b32_e32 v23, v171
	v_mov_b32_e32 v24, v172
	v_mov_b32_e32 v25, v173
	v_mov_b32_e32 v26, v174
	v_mov_b32_e32 v27, v175
	v_pk_mul_f32 v[20:21], v[20:21], v[2:3]
	v_pk_mul_f32 v[24:25], v[24:25], v[6:7]
	v_pk_mul_f32 v[26:27], v[26:27], v[8:9]
	v_pk_mul_f32 v[28:29], v[24:25], v[10:11]
	s_nop 0
	v_and_b32_sdwa v30, v29, v226 dst_sel:DWORD dst_unused:UNUSED_PAD src0_sel:WORD_1 src1_sel:DWORD
	v_and_b32_sdwa v31, v28, v226 dst_sel:DWORD dst_unused:UNUSED_PAD src0_sel:WORD_1 src1_sel:DWORD
	v_add3_u32 v29, v29, v30, s9
	v_add3_u32 v28, v28, v31, s9
	v_pk_mul_f32 v[30:31], v[26:27], v[12:13]
	v_and_b32_e32 v29, 0xffff0000, v29
	v_and_b32_sdwa v32, v31, v226 dst_sel:DWORD dst_unused:UNUSED_PAD src0_sel:WORD_1 src1_sel:DWORD
	v_and_b32_sdwa v33, v30, v226 dst_sel:DWORD dst_unused:UNUSED_PAD src0_sel:WORD_1 src1_sel:DWORD
	v_add3_u32 v31, v31, v32, s9
	v_add3_u32 v30, v30, v33, s9
	v_pk_mul_f32 v[32:33], v[20:21], v[14:15]
	v_and_b32_e32 v28, 0xffff0000, v28
	v_and_b32_sdwa v34, v33, v226 dst_sel:DWORD dst_unused:UNUSED_PAD src0_sel:WORD_1 src1_sel:DWORD
	v_and_b32_sdwa v35, v32, v226 dst_sel:DWORD dst_unused:UNUSED_PAD src0_sel:WORD_1 src1_sel:DWORD
	v_add3_u32 v33, v33, v34, s9
	v_add3_u32 v32, v32, v35, s9
	v_and_b32_e32 v33, 0xffff0000, v33
	v_and_b32_e32 v32, 0xffff0000, v32
	v_pk_fma_f32 v[34:35], v[20:21], v[14:15], v[32:33] neg_lo:[0,0,1] neg_hi:[0,0,1]
	v_pk_mul_f32 v[20:21], v[22:23], v[4:5]
	v_pk_fma_f32 v[24:25], v[24:25], v[10:11], v[28:29] neg_lo:[0,0,1] neg_hi:[0,0,1]
	v_pk_mul_f32 v[22:23], v[20:21], v[16:17]
	v_and_b32_e32 v31, 0xffff0000, v31
	v_and_b32_sdwa v36, v23, v226 dst_sel:DWORD dst_unused:UNUSED_PAD src0_sel:WORD_1 src1_sel:DWORD
	v_and_b32_sdwa v37, v22, v226 dst_sel:DWORD dst_unused:UNUSED_PAD src0_sel:WORD_1 src1_sel:DWORD
	v_add3_u32 v23, v23, v36, s9
	v_add3_u32 v22, v22, v37, s9
	v_and_b32_e32 v37, 0xffff0000, v23
	v_and_b32_e32 v36, 0xffff0000, v22
	v_and_b32_e32 v30, 0xffff0000, v30
	v_pk_fma_f32 v[38:39], v[20:21], v[16:17], v[36:37] neg_lo:[0,0,1] neg_hi:[0,0,1]
	v_cvt_pk_bf16_f32 v20, v28, v29
	v_lshlrev_b32_e32 v28, 4, v40
	v_pk_fma_f32 v[26:27], v[26:27], v[12:13], v[30:31] neg_lo:[0,0,1] neg_hi:[0,0,1]
	v_cvt_pk_bf16_f32 v21, v30, v31
	v_cvt_pk_bf16_f32 v22, v32, v33
	v_cvt_pk_bf16_f32 v23, v36, v37
	v_add3_u32 v29, 0, v19, v28
	ds_write_b128 v29, v[20:23]
	v_cvt_pk_bf16_f32 v20, v24, v25
	v_cvt_pk_bf16_f32 v21, v26, v27
	v_cvt_pk_bf16_f32 v22, v34, v35
	v_cvt_pk_bf16_f32 v23, v38, v39
	v_add3_u32 v19, s27, v19, v28
	s_movk_i32 s27, 0xfff
	ds_write_b128 v19, v[20:23]
	v_add_u32_e32 v18, 0x200, v18
	v_ashrrev_i32_e32 v19, 7, v18
	v_bitop3_b32 v40, v19, v89, 15 bitop3:0x6c
	v_lshlrev_b32_e32 v19, 11, v19
	s_add_i32 s27, 0, 0x12000
	s_waitcnt vmcnt(2)
	v_mov_b32_e32 v20, v176
	v_mov_b32_e32 v21, v177
	v_mov_b32_e32 v22, v178
	v_mov_b32_e32 v23, v179
	v_mov_b32_e32 v24, v180
	v_mov_b32_e32 v25, v181
	v_mov_b32_e32 v26, v182
	v_mov_b32_e32 v27, v183
	v_pk_mul_f32 v[20:21], v[20:21], v[2:3]
	v_pk_mul_f32 v[24:25], v[24:25], v[6:7]
	v_pk_mul_f32 v[26:27], v[26:27], v[8:9]
	v_pk_mul_f32 v[28:29], v[24:25], v[10:11]
	s_nop 0
	v_and_b32_sdwa v30, v29, v226 dst_sel:DWORD dst_unused:UNUSED_PAD src0_sel:WORD_1 src1_sel:DWORD
	v_and_b32_sdwa v31, v28, v226 dst_sel:DWORD dst_unused:UNUSED_PAD src0_sel:WORD_1 src1_sel:DWORD
	v_add3_u32 v29, v29, v30, s9
	v_add3_u32 v28, v28, v31, s9
	v_pk_mul_f32 v[30:31], v[26:27], v[12:13]
	v_and_b32_e32 v29, 0xffff0000, v29
	v_and_b32_sdwa v32, v31, v226 dst_sel:DWORD dst_unused:UNUSED_PAD src0_sel:WORD_1 src1_sel:DWORD
	v_and_b32_sdwa v33, v30, v226 dst_sel:DWORD dst_unused:UNUSED_PAD src0_sel:WORD_1 src1_sel:DWORD
	v_add3_u32 v31, v31, v32, s9
	v_add3_u32 v30, v30, v33, s9
	v_pk_mul_f32 v[32:33], v[20:21], v[14:15]
	v_and_b32_e32 v28, 0xffff0000, v28
	v_and_b32_sdwa v34, v33, v226 dst_sel:DWORD dst_unused:UNUSED_PAD src0_sel:WORD_1 src1_sel:DWORD
	v_and_b32_sdwa v35, v32, v226 dst_sel:DWORD dst_unused:UNUSED_PAD src0_sel:WORD_1 src1_sel:DWORD
	v_add3_u32 v33, v33, v34, s9
	v_add3_u32 v32, v32, v35, s9
	v_and_b32_e32 v33, 0xffff0000, v33
	v_and_b32_e32 v32, 0xffff0000, v32
	v_pk_fma_f32 v[34:35], v[20:21], v[14:15], v[32:33] neg_lo:[0,0,1] neg_hi:[0,0,1]
	v_pk_mul_f32 v[20:21], v[22:23], v[4:5]
	v_pk_fma_f32 v[24:25], v[24:25], v[10:11], v[28:29] neg_lo:[0,0,1] neg_hi:[0,0,1]
	v_pk_mul_f32 v[22:23], v[20:21], v[16:17]
	v_and_b32_e32 v31, 0xffff0000, v31
	v_and_b32_sdwa v36, v23, v226 dst_sel:DWORD dst_unused:UNUSED_PAD src0_sel:WORD_1 src1_sel:DWORD
	v_and_b32_sdwa v37, v22, v226 dst_sel:DWORD dst_unused:UNUSED_PAD src0_sel:WORD_1 src1_sel:DWORD
	v_add3_u32 v23, v23, v36, s9
	v_add3_u32 v22, v22, v37, s9
	v_and_b32_e32 v37, 0xffff0000, v23
	v_and_b32_e32 v36, 0xffff0000, v22
	v_and_b32_e32 v30, 0xffff0000, v30
	v_pk_fma_f32 v[38:39], v[20:21], v[16:17], v[36:37] neg_lo:[0,0,1] neg_hi:[0,0,1]
	v_cvt_pk_bf16_f32 v20, v28, v29
	v_lshlrev_b32_e32 v28, 4, v40
	v_pk_fma_f32 v[26:27], v[26:27], v[12:13], v[30:31] neg_lo:[0,0,1] neg_hi:[0,0,1]
	v_cvt_pk_bf16_f32 v21, v30, v31
	v_cvt_pk_bf16_f32 v22, v32, v33
	v_cvt_pk_bf16_f32 v23, v36, v37
	v_add3_u32 v29, 0, v19, v28
	ds_write_b128 v29, v[20:23]
	v_cvt_pk_bf16_f32 v20, v24, v25
	v_cvt_pk_bf16_f32 v21, v26, v27
	v_cvt_pk_bf16_f32 v22, v34, v35
	v_cvt_pk_bf16_f32 v23, v38, v39
	v_add3_u32 v19, s27, v19, v28
	s_movk_i32 s27, 0xfff
	ds_write_b128 v19, v[20:23]
	v_add_u32_e32 v18, 0x200, v18
	v_ashrrev_i32_e32 v19, 7, v18
	v_bitop3_b32 v40, v19, v89, 15 bitop3:0x6c
	v_lshlrev_b32_e32 v19, 11, v19
	s_add_i32 s27, 0, 0x12000
	s_waitcnt vmcnt(0)
	v_mov_b32_e32 v20, v184
	v_mov_b32_e32 v21, v185
	v_mov_b32_e32 v22, v186
	v_mov_b32_e32 v23, v187
	v_mov_b32_e32 v24, v188
	v_mov_b32_e32 v25, v189
	v_mov_b32_e32 v26, v190
	v_mov_b32_e32 v27, v191
	v_pk_mul_f32 v[20:21], v[20:21], v[2:3]
	v_pk_mul_f32 v[24:25], v[24:25], v[6:7]
	v_pk_mul_f32 v[26:27], v[26:27], v[8:9]
	v_pk_mul_f32 v[28:29], v[24:25], v[10:11]
	s_nop 0
	v_and_b32_sdwa v30, v29, v226 dst_sel:DWORD dst_unused:UNUSED_PAD src0_sel:WORD_1 src1_sel:DWORD
	v_and_b32_sdwa v31, v28, v226 dst_sel:DWORD dst_unused:UNUSED_PAD src0_sel:WORD_1 src1_sel:DWORD
	v_add3_u32 v29, v29, v30, s9
	v_add3_u32 v28, v28, v31, s9
	v_pk_mul_f32 v[30:31], v[26:27], v[12:13]
	v_and_b32_e32 v29, 0xffff0000, v29
	v_and_b32_sdwa v32, v31, v226 dst_sel:DWORD dst_unused:UNUSED_PAD src0_sel:WORD_1 src1_sel:DWORD
	v_and_b32_sdwa v33, v30, v226 dst_sel:DWORD dst_unused:UNUSED_PAD src0_sel:WORD_1 src1_sel:DWORD
	v_add3_u32 v31, v31, v32, s9
	v_add3_u32 v30, v30, v33, s9
	v_pk_mul_f32 v[32:33], v[20:21], v[14:15]
	v_and_b32_e32 v28, 0xffff0000, v28
	v_and_b32_sdwa v34, v33, v226 dst_sel:DWORD dst_unused:UNUSED_PAD src0_sel:WORD_1 src1_sel:DWORD
	v_and_b32_sdwa v35, v32, v226 dst_sel:DWORD dst_unused:UNUSED_PAD src0_sel:WORD_1 src1_sel:DWORD
	v_add3_u32 v33, v33, v34, s9
	v_add3_u32 v32, v32, v35, s9
	v_and_b32_e32 v33, 0xffff0000, v33
	v_and_b32_e32 v32, 0xffff0000, v32
	v_pk_fma_f32 v[34:35], v[20:21], v[14:15], v[32:33] neg_lo:[0,0,1] neg_hi:[0,0,1]
	v_pk_mul_f32 v[20:21], v[22:23], v[4:5]
	v_pk_fma_f32 v[24:25], v[24:25], v[10:11], v[28:29] neg_lo:[0,0,1] neg_hi:[0,0,1]
	v_pk_mul_f32 v[22:23], v[20:21], v[16:17]
	v_and_b32_e32 v31, 0xffff0000, v31
	v_and_b32_sdwa v36, v23, v226 dst_sel:DWORD dst_unused:UNUSED_PAD src0_sel:WORD_1 src1_sel:DWORD
	v_and_b32_sdwa v37, v22, v226 dst_sel:DWORD dst_unused:UNUSED_PAD src0_sel:WORD_1 src1_sel:DWORD
	v_add3_u32 v23, v23, v36, s9
	v_add3_u32 v22, v22, v37, s9
	v_and_b32_e32 v37, 0xffff0000, v23
	v_and_b32_e32 v36, 0xffff0000, v22
	v_and_b32_e32 v30, 0xffff0000, v30
	v_pk_fma_f32 v[38:39], v[20:21], v[16:17], v[36:37] neg_lo:[0,0,1] neg_hi:[0,0,1]
	v_cvt_pk_bf16_f32 v20, v28, v29
	v_lshlrev_b32_e32 v28, 4, v40
	v_pk_fma_f32 v[26:27], v[26:27], v[12:13], v[30:31] neg_lo:[0,0,1] neg_hi:[0,0,1]
	v_cvt_pk_bf16_f32 v21, v30, v31
	v_cvt_pk_bf16_f32 v22, v32, v33
	v_cvt_pk_bf16_f32 v23, v36, v37
	v_add3_u32 v29, 0, v19, v28
	ds_write_b128 v29, v[20:23]
	v_cvt_pk_bf16_f32 v20, v24, v25
	v_cvt_pk_bf16_f32 v21, v26, v27
	v_cvt_pk_bf16_f32 v22, v34, v35
	v_cvt_pk_bf16_f32 v23, v38, v39
	v_add3_u32 v19, s27, v19, v28
	s_movk_i32 s27, 0xfff
	ds_write_b128 v19, v[20:23]
	v_add_u32_e32 v18, 0x200, v18
